# speedup vs baseline: 1.0045x; 1.0045x over previous
_Z14rnn_b4s_kernelPKfS0_S0_S0_S0_S0_S0_Pf:
	s_load_dwordx8 s[12:19], s[0:1], 0x0
	s_load_dwordx8 s[4:11], s[0:1], 0x20
	v_readfirstlane_b32 s0, v0
	s_lshr_b32 s24, s0, 6
	s_lshl_b32 s0, s2, 5
	s_and_b32 s0, s0, 0xe0
	s_lshr_b32 s1, s2, 3
	s_add_i32 s0, s0, s1
	s_lshl_b32 s0, s0, 4
	s_lshl_b32 s1, s24, 2
	s_mov_b32 s23, 0
	s_add_i32 s20, s1, s0
	s_mov_b32 s21, s23
	s_lshl_b64 s[0:1], s[20:21], 15
	v_and_b32_e32 v174, 63, v0
	s_mulk_i32 s24, 0x4400
	s_waitcnt lgkmcnt(0)
	s_add_u32 s0, s12, s0
	s_addc_u32 s1, s13, s1
	v_lshlrev_b32_e32 v2, 4, v174
	v_mov_b32_e32 v3, 0
	s_mov_b32 m0, s24
	v_and_b32_e32 v64, 1, v0
	v_and_b32_e32 v18, 2, v0
	v_lshl_add_u64 v[166:167], s[0:1], 0, v[2:3]
	global_load_lds_dwordx4 v2, s[0:1] nt
	v_lshlrev_b32_e32 v4, 6, v64
	v_and_b32_e32 v2, 48, v0
	v_lshlrev_b32_e32 v12, 2, v18
	v_lshlrev_b32_e32 v66, 1, v0
	v_and_b32_e32 v1, 15, v0
	v_or3_b32 v65, v4, v12, v2
	v_and_b32_e32 v4, 32, v66
	v_mov_b32_e32 v5, v3
	v_lshl_add_u64 v[14:15], s[14:15], 0, v[4:5]
	v_lshlrev_b32_e32 v4, 6, v1
	v_lshl_add_u64 v[16:17], v[14:15], 0, v[4:5]
	v_add_u32_e32 v18, -1, v18
	v_lshl_add_u64 v[20:21], s[16:17], 0, v[2:3]
	global_load_dwordx4 v[4:7], v[16:17], off offset:16
	global_load_dwordx4 v[8:11], v[16:17], off
	v_lshlrev_b32_e32 v16, 7, v1
	v_mov_b32_e32 v17, v3
	v_bitop3_b32 v19, v0, 2, v0 bitop3:0xc
	v_and_b32_e32 v18, 2, v18
	v_lshl_add_u64 v[16:17], v[20:21], 0, v[16:17]
	v_mov_b32_e32 v13, v3
	v_lshlrev_b32_e32 v22, 2, v19
	v_mov_b32_e32 v23, v3
	v_lshlrev_b32_e32 v26, 2, v18
	v_mov_b32_e32 v27, v3
	v_or_b32_e32 v1, 16, v1
	v_lshl_add_u64 v[24:25], v[16:17], 0, v[12:13]
	v_lshl_add_u64 v[46:47], v[16:17], 0, v[22:23]
	v_lshl_add_u64 v[48:49], v[16:17], 0, v[26:27]
	v_lshlrev_b32_e32 v16, 6, v1
	v_mov_b32_e32 v17, v3
	v_lshl_add_u64 v[14:15], v[14:15], 0, v[16:17]
	global_load_dwordx4 v[16:19], v[14:15], off offset:16
	global_load_dwordx4 v[42:45], v[14:15], off
	v_lshlrev_b32_e32 v14, 7, v1
	v_mov_b32_e32 v15, v3
	v_lshl_add_u64 v[14:15], v[20:21], 0, v[14:15]
	v_lshl_add_u64 v[12:13], v[14:15], 0, v[12:13]
	v_lshl_add_u64 v[50:51], v[14:15], 0, v[22:23]
	v_lshl_add_u64 v[14:15], v[14:15], 0, v[26:27]
	global_load_dwordx2 v[168:169], v65, s[6:7] offset:128
	global_load_dwordx2 v[170:171], v65, s[6:7]
	global_load_dwordx2 v[20:21], v[12:13], off
	global_load_dwordx2 v[22:23], v[14:15], off offset:64
	global_load_dwordx2 v[52:53], v[50:51], off
	global_load_dwordx2 v[54:55], v[12:13], off offset:64
	global_load_dwordx2 v[56:57], v[48:49], off offset:64
	global_load_dwordx2 v[58:59], v[46:47], off
	global_load_dwordx2 v[60:61], v[24:25], off offset:64
	global_load_dwordx2 v[62:63], v[24:25], off
	global_load_dwordx4 v[26:29], v2, s[4:5] offset:64
	global_load_dwordx4 v[34:37], v2, s[4:5]
	global_load_dwordx4 v[30:33], v2, s[18:19] offset:64
	global_load_dwordx4 v[38:41], v2, s[18:19]
	s_mov_b64 s[0:1], 0x8000
	v_lshl_add_u64 v[2:3], v[166:167], 0, s[0:1]
	s_add_i32 m0, s24, 0x440
	s_mov_b64 s[0:1], 0x10000
	global_load_lds_dwordx4 v[2:3], off nt
	v_lshl_add_u64 v[2:3], v[166:167], 0, s[0:1]
	s_add_i32 m0, s24, 0x880
	s_mov_b64 s[0:1], 0x18000
	global_load_lds_dwordx4 v[2:3], off nt
	v_lshl_add_u64 v[2:3], v[166:167], 0, s[0:1]
	s_add_i32 m0, s24, 0xcc0
	s_mov_b64 s[0:1], 0x400
	s_load_dwordx2 s[2:3], s[8:9], 0x0
	global_load_lds_dwordx4 v[2:3], off nt
	s_add_i32 m0, s24, 0x1100
	v_lshl_add_u64 v[2:3], v[166:167], 0, s[0:1]
	s_mov_b64 s[0:1], 0x8400
	global_load_lds_dwordx4 v[2:3], off nt
	v_lshl_add_u64 v[2:3], v[166:167], 0, s[0:1]
	s_add_i32 m0, s24, 0x1540
	s_mov_b64 s[0:1], 0x10400
	global_load_lds_dwordx4 v[2:3], off nt
	v_lshl_add_u64 v[2:3], v[166:167], 0, s[0:1]
	s_add_i32 m0, s24, 0x1980
	s_mov_b64 s[0:1], 0x18400
	global_load_lds_dwordx4 v[2:3], off nt
	v_lshl_add_u64 v[2:3], v[166:167], 0, s[0:1]
	s_add_i32 m0, s24, 0x1dc0
	global_load_lds_dwordx4 v[2:3], off nt
	s_mov_b64 s[0:1], 0x800
	s_add_i32 m0, s24, 0x2200
	v_lshl_add_u64 v[2:3], v[166:167], 0, s[0:1]
	global_load_lds_dwordx4 v[2:3], off nt
	s_mov_b64 s[0:1], 0x8800
	s_add_i32 m0, s24, 0x2640
	v_lshl_add_u64 v[2:3], v[166:167], 0, s[0:1]
	global_load_lds_dwordx4 v[2:3], off nt
	s_mov_b64 s[0:1], 0x10800
	s_add_i32 m0, s24, 0x2a80
	v_lshl_add_u64 v[2:3], v[166:167], 0, s[0:1]
	global_load_lds_dwordx4 v[2:3], off nt
	s_mov_b64 s[0:1], 0x18800
	s_add_i32 m0, s24, 0x2ec0
	v_lshl_add_u64 v[2:3], v[166:167], 0, s[0:1]
	global_load_lds_dwordx4 v[2:3], off nt
	s_mov_b64 s[0:1], 0xc00
	s_add_i32 m0, s24, 0x3300
	v_lshl_add_u64 v[2:3], v[166:167], 0, s[0:1]
	global_load_lds_dwordx4 v[2:3], off nt
	s_mov_b64 s[0:1], 0x8c00
	s_add_i32 m0, s24, 0x3740
	v_lshl_add_u64 v[2:3], v[166:167], 0, s[0:1]
	global_load_lds_dwordx4 v[2:3], off nt
	s_mov_b64 s[0:1], 0x10c00
	s_add_i32 m0, s24, 0x3b80
	v_lshl_add_u64 v[2:3], v[166:167], 0, s[0:1]
	global_load_lds_dwordx4 v[2:3], off nt
	s_mov_b64 s[0:1], 0x18c00
	s_add_i32 m0, s24, 0x3fc0
	v_lshl_add_u64 v[2:3], v[166:167], 0, s[0:1]
	global_load_lds_dwordx4 v[2:3], off nt
	s_waitcnt lgkmcnt(0)
	v_mov_b64_e32 v[172:173], s[2:3]
	s_mov_b32 s2, 0x4038aa3b
	s_waitcnt vmcnt(15)
	s_waitcnt vmcnt(15)
	s_nop 0
	v_fma_mixlo_f16 v2, v8, s2, 0
	v_cmp_gt_u32_e64 s[0:1], 32, v174
	v_cmp_lt_u32_e32 vcc, 31, v174
	s_movk_i32 s5, 0x440
	v_cndmask_b32_e64 v12, 0, v2, s[0:1]
	v_cndmask_b32_e32 v14, 0, v2, vcc
	v_fma_mixlo_f16 v2, v9, s2, 0
	s_mov_b32 s4, 0xc0b8aa3b
	v_cndmask_b32_e64 v13, 0, v2, s[0:1]
	v_cndmask_b32_e32 v15, 0, v2, vcc
	v_pk_mov_b32 v[2:3], v[62:63], v[60:61] op_sel:[1,0]
	v_fma_mixlo_f16 v4, v4, s2, 0
	v_pk_mul_f32 v[2:3], v[2:3], s[4:5] op_sel_hi:[1,0]
	v_fma_mixlo_f16 v8, v11, s2, 0
	v_cndmask_b32_e64 v25, 0, v4, s[0:1]
	v_cndmask_b32_e32 v46, 0, v4, vcc
	v_fma_mixlo_f16 v4, v5, s2, 0
	v_fma_mixlo_f16 v1, v62, s4, 0
	v_cvt_pk_f16_f32 v3, v2, v3
	v_cndmask_b32_e64 v11, 0, v8, s[0:1]
	v_cndmask_b32_e32 v24, 0, v8, vcc
	v_pk_mov_b32 v[8:9], v[60:61], v[58:59] op_sel:[1,0]
	v_cndmask_b32_e64 v47, 0, v4, s[0:1]
	v_cndmask_b32_e32 v48, 0, v4, vcc
	v_pk_mov_b32 v[4:5], v[58:59], v[56:57] op_sel:[1,0]
	v_pack_b32_f16 v2, v1, v3
	v_fma_mixlo_f16 v1, v10, s2, 0
	v_pk_mul_f32 v[8:9], v[8:9], s[4:5] op_sel_hi:[1,0]
	v_pk_mul_f32 v[4:5], v[4:5], s[4:5] op_sel_hi:[1,0]
	v_cndmask_b32_e64 v10, 0, v1, s[0:1]
	v_cvt_pk_f16_f32 v8, v8, v9
	v_cvt_pk_f16_f32 v5, v4, v5
	v_fma_mixlo_f16 v6, v6, s2, 0
	v_fma_mixlo_f16 v50, v7, s2, 0
	v_alignbit_b32 v3, v8, v3, 16
	v_alignbit_b32 v4, v5, v8, 16
	v_cndmask_b32_e64 v8, 0, v6, s[0:1]
	v_cndmask_b32_e32 v49, 0, v6, vcc
	v_cndmask_b32_e64 v6, 0, v50, s[0:1]
	v_pack_b32_f16 v7, v10, v11
	v_cndmask_b32_e32 v10, 0, v50, vcc
	v_pack_b32_f16 v9, v8, v6
	v_pack_b32_f16 v6, v12, v13
	v_pack_b32_f16 v13, v49, v10
	v_pack_b32_f16 v10, v14, v15
	v_fma_mixlo_f16 v14, v42, s2, 0
	v_pack_b32_f16 v8, v25, v47
	v_pack_b32_f16 v12, v46, v48
	v_cndmask_b32_e64 v46, 0, v14, s[0:1]
	v_cndmask_b32_e32 v47, 0, v14, vcc
	v_fma_mixlo_f16 v14, v43, s2, 0
	v_cndmask_b32_e32 v1, 0, v1, vcc
	v_pack_b32_f16 v11, v1, v24
	v_fma_mixlo_f16 v24, v45, s2, 0
	v_cndmask_b32_e64 v45, 0, v24, s[0:1]
	v_cndmask_b32_e32 v50, 0, v24, vcc
	v_pk_mov_b32 v[24:25], v[52:53], v[22:23] op_sel:[1,0]
	v_fma_mixlo_f16 v16, v16, s2, 0
	v_pk_mul_f32 v[24:25], v[24:25], s[4:5] op_sel_hi:[1,0]
	v_lshrrev_b32_e32 v5, 16, v5
	v_cvt_pk_f16_f32 v24, v24, v25
	v_cndmask_b32_e64 v25, 0, v16, s[0:1]
	v_cndmask_b32_e32 v42, 0, v16, vcc
	v_fma_mixlo_f16 v16, v17, s2, 0
	v_fma_mixhi_f16 v5, v57, s4, 0
	v_cndmask_b32_e64 v43, 0, v16, s[0:1]
	v_cndmask_b32_e32 v51, 0, v16, vcc
	v_pk_mov_b32 v[16:17], v[22:23], v[20:21] op_sel:[1,0]
	v_cndmask_b32_e64 v48, 0, v14, s[0:1]
	v_cndmask_b32_e32 v49, 0, v14, vcc
	v_pk_mov_b32 v[14:15], v[54:55], v[52:53] op_sel:[1,0]
	v_pk_mul_f32 v[16:17], v[16:17], s[4:5] op_sel_hi:[1,0]
	s_mov_b32 s12, 0xb800b800
	v_pk_mul_f32 v[14:15], v[14:15], s[4:5] op_sel_hi:[1,0]
	v_cvt_pk_f16_f32 v17, v16, v17
	s_mov_b32 s14, s12
	s_mov_b32 s15, s12
	v_fma_mixlo_f16 v1, v54, s4, 0
	v_cvt_pk_f16_f32 v15, v14, v15
	v_alignbit_b32 v16, v17, v24, 16
	v_lshrrev_b32_e32 v17, 16, v17
	v_pk_add_f32 v[36:37], v[40:41], v[36:37]
	v_pk_add_f32 v[34:35], v[38:39], v[34:35]
	s_mov_b32 s13, s12
	v_mov_b64_e32 v[40:41], s[14:15]
	v_pack_b32_f16 v14, v1, v15
	v_alignbit_b32 v15, v24, v15, 16
	v_fma_mixhi_f16 v17, v21, s4, 0
	v_pk_mul_f32 v[36:37], v[36:37], s[2:3] op_sel_hi:[1,0]
	v_pk_mul_f32 v[34:35], v[34:35], s[2:3] op_sel_hi:[1,0]
	v_mov_b64_e32 v[38:39], s[12:13]
	v_fma_mixlo_f16 v1, v44, s2, 0
	v_fma_mixlo_f16 v18, v18, s2, 0
	v_mfma_f32_16x16x32_f16 v[34:37], v[2:5], v[38:41], v[34:37]
	v_fma_mixlo_f16 v23, v19, s2, 0
	v_and_b32_e32 v176, 3, v0
	v_cndmask_b32_e64 v44, 0, v1, s[0:1]
	v_cndmask_b32_e32 v1, 0, v1, vcc
	v_cndmask_b32_e64 v20, 0, v18, s[0:1]
	v_cndmask_b32_e32 v22, 0, v18, vcc
	v_cndmask_b32_e64 v18, 0, v23, s[0:1]
	v_cndmask_b32_e32 v23, 0, v23, vcc
	v_pk_add_f32 v[28:29], v[32:33], v[28:29]
	v_pk_add_f32 v[26:27], v[30:31], v[26:27]
	v_cmp_gt_u32_e32 vcc, 2, v176
	v_cmp_eq_u32_e64 s[0:1], 0, v64
	v_bfe_u32 v175, v0, 2, 2
	v_and_b32_e32 v95, 0x60, v66
	v_or_b32_e32 v95, s24, v95
	v_mad_u32_u24 v94, v175, s5, v95
	s_waitcnt vmcnt(12)
	ds_read_b128 v[82:85], v94
	ds_read_b128 v[86:89], v94 offset:16
	v_pack_b32_f16 v21, v20, v18
	v_pack_b32_f16 v20, v25, v43
	v_pack_b32_f16 v25, v22, v23
	v_pack_b32_f16 v23, v1, v50
	v_pk_mul_f32 v[28:29], v[28:29], s[2:3] op_sel_hi:[1,0]
	v_pk_mul_f32 v[26:27], v[26:27], s[2:3] op_sel_hi:[1,0]
	v_mov_b32_e32 v1, 0xf149f2ca
	s_and_b64 s[2:3], s[0:1], vcc
	v_bitop3_b32 v0, v0, 2, 3 bitop3:0x6c
	v_mfma_f32_16x16x32_f16 v[30:33], v[14:17], v[38:41], v[26:29]
	v_pack_b32_f16 v19, v44, v45
	v_pack_b32_f16 v18, v46, v48
	v_pack_b32_f16 v24, v42, v51
	v_cndmask_b32_e64 v26, v1, v34, s[2:3]
	v_cndmask_b32_e64 v27, v1, v35, s[2:3]
	v_cmp_gt_u32_e64 s[2:3], 2, v0
	s_and_b64 s[0:1], s[0:1], s[2:3]
	v_cndmask_b32_e64 v28, v1, v36, s[0:1]
	v_cndmask_b32_e64 v29, v1, v37, s[0:1]
	v_cmp_eq_u32_e64 s[0:1], 1, v64
	s_and_b64 vcc, s[0:1], vcc
	v_and_b32_e32 v0, 0x60, v66
	v_cndmask_b32_e32 v30, v1, v30, vcc
	v_cndmask_b32_e32 v31, v1, v31, vcc
	s_and_b64 vcc, s[0:1], s[2:3]
	v_or_b32_e32 v0, s24, v0
	v_mov_b32_e32 v34, 0x38003800
	v_pack_b32_f16 v22, v47, v49
	v_cndmask_b32_e32 v32, v1, v32, vcc
	v_cndmask_b32_e32 v33, v1, v33, vcc
	v_mad_u32_u24 v177, v175, s5, v0
	s_mov_b64 s[0:1], 0x1000
	s_mov_b64 s[2:3], 0x9000
	s_mov_b64 s[4:5], 0x11000
	s_mov_b64 s[6:7], 0x19000
	s_mov_b32 s8, 0
	v_mov_b32_e32 v35, v34
	v_mov_b32_e32 v37, v34
	v_mov_b32_e32 v36, v34
	v_mov_b32_e32 v94, v177
	s_waitcnt lgkmcnt(0)
	v_cvt_pk_f16_f32 v78, v82, v83
	v_cvt_pk_f16_f32 v79, v84, v85
	v_cvt_pk_f16_f32 v80, v86, v87
	v_cvt_pk_f16_f32 v81, v88, v89
	ds_read_b128 v[82:85], v177 offset:128
	ds_read_b128 v[86:89], v177 offset:144
	v_mfma_f32_16x16x32_f16 v[46:49], v[6:9], v[78:81], v[26:29]
	v_mfma_f32_16x16x32_f16 v[50:53], v[18:21], v[78:81], v[30:33]
	v_mfma_f32_16x16x32_f16 v[54:57], v[10:13], v[78:81], v[26:29]
	v_mfma_f32_16x16x32_f16 v[58:61], v[22:25], v[78:81], v[30:33]
	s_waitcnt lgkmcnt(0)
	v_cvt_pk_f16_f32 v78, v82, v83
	v_cvt_pk_f16_f32 v79, v84, v85
	v_cvt_pk_f16_f32 v80, v86, v87
	v_cvt_pk_f16_f32 v81, v88, v89
	s_nop 1
	.p2align 6
